# both layers MoE weight conversion deferred out of the prologue/phase 0 into the dense GEMM phases (half the workgroups convert before, half after their units); prologue converts only W_in and the squa
# speedup vs baseline: 1.0271x; 1.0130x over previous
; #define LAS __attribute__((address_space(3)))
; __device__ __forceinline__ void wg_convert_layer(Frame& F, int l) {
;     __syncthreads();
;     for (int it = F.gw >> 3; it < WG_ITEMS_PER_LAYER; it += F.G) wg_conv_item(F, l, it);
; }
; __device__ __forceinline__ void p0_prologue(Frame& F) {
;     LAS float* scr = (LAS float*)(F.lds + F.wave * 16384);
;     wg_convert_layer(F, 0);
.LBB0_8:
	s_or_b64 exec, exec, s[6:7]
	s_load_dwordx2 s[74:75], s[92:93], 0xe8
	s_lshl_b32 s6, s10, 3
	v_readlane_b32 s7, v251, 2
	s_add_i32 s6, s6, s7
	s_lshl_b32 s84, s68, 3
	v_writelane_b32 v251, s6, 3
	s_waitcnt lgkmcnt(0)
	s_cmp_lt_i32 s74, 1
	v_writelane_b32 v251, s87, 4
	s_cselect_b64 s[6:7], -1, 0
	s_cmp_gt_i32 s75, 0
	v_writelane_b32 v251, s72, 5
	s_cselect_b64 s[8:9], -1, 0
	s_and_b64 s[12:13], s[6:7], s[8:9]
	v_writelane_b32 v251, s73, 6
	v_writelane_b32 v251, s74, 7
	s_and_b64 vcc, exec, s[12:13]
	s_nop 0
	v_writelane_b32 v251, s75, 8
	s_cbranch_vccz .LBB0_225
	v_readlane_b32 s6, v251, 3
	s_ashr_i32 s30, s6, 3
	s_mov_b32 s94, s68
	s_mov_b32 s90, s84
	s_cmpk_gt_i32 s30, 0x20f
	s_barrier
	s_cbranch_scc1 .LBB0_161
	s_add_u32 s31, s0, 0x18500000
	v_readlane_b32 s6, v251, 2
	s_addc_u32 s34, s1, 0
	s_lshl_b32 s35, s6, 3
	s_add_i32 s36, s6, 8
	s_add_i32 s37, s6, 16
	s_add_i32 s38, s6, 24
	s_add_u32 s39, s0, 0x8500000
	s_load_dwordx2 s[8:9], s[92:93], 0x98
	s_load_dwordx2 s[10:11], s[92:93], 0xd0
	s_load_dwordx2 s[14:15], s[92:93], 0x58
	s_addc_u32 s40, s1, 0
	s_add_u32 s41, s0, 0x100000
	s_addc_u32 s42, s1, 0
	s_load_dwordx2 s[18:19], s[92:93], 0x18
	s_waitcnt lgkmcnt(0)
	s_cmp_lg_u64 s[8:9], 0
	s_cselect_b64 s[16:17], -1, 0
	s_cmp_eq_u64 s[14:15], 0
	s_cselect_b64 s[20:21], -1, 0
	s_lshl_b32 s6, s30, 5
	s_lshl_b32 s43, s30, 8
	s_lshl_b32 s44, s94, 8
	s_add_i32 s45, s6, 0xffffe600
	s_lshl_b32 s46, s94, 5
	s_movk_i32 s47, 0x2000
	s_movk_i32 s48, 0x4000
	s_movk_i32 s49, 0x6000
	s_mov_b32 s50, 0x8000
	s_mov_b32 s51, 0xa000
	s_mov_b32 s52, 0xc000
	s_mov_b32 s53, 0xe000
	s_mov_b32 s54, 0x80000
	s_mov_b32 s55, 0x82000
	s_mov_b32 s56, 0x84000
	s_mov_b32 s57, 0x86000
	s_mov_b32 s58, 0x88000
	s_mov_b32 s59, 0x100000
	s_mov_b32 s60, 0x102000
	s_mov_b32 s61, 0x104000
	s_mov_b32 s62, 0x106000
	s_mov_b32 s63, 0x108000
	s_mov_b32 s64, 0x180000
	s_mov_b32 s65, 0x182000
	s_mov_b32 s66, 0x184000
	s_mov_b32 s67, 0x186000
	s_mov_b32 s68, 0x188000
	v_mov_b32_e32 v67, 0
	s_mov_b32 s69, 0x20000
	s_mov_b32 s70, 0x1ce000
	s_mov_b32 s71, 0x341000
	s_mov_b32 s72, 0x347000
	s_mov_b32 s73, 0x34e000
	s_mov_b32 s74, 0x354000
	s_mov_b32 s75, 0x35b000
	s_mov_b32 s76, 0x361000
	s_mov_b32 s77, 0x368000
	s_mov_b32 s78, 0x36e000
	s_mov_b32 s79, 0x4e1000
	s_mov_b32 s80, 0x4e8000
	s_mov_b32 s81, 0x4ee000
	s_mov_b32 s82, 0x4f5000
	s_mov_b32 s83, 0x4fb000
	s_mov_b32 s84, 0x502000
	s_mov_b32 s85, 0x508000
	s_mov_b32 s86, 0x50f000
	s_mov_b32 s23, 0
	s_branch .LBB0_12
.LBB0_11:
	s_add_i32 s30, s30, s94
	s_add_i32 s43, s43, s44
	s_add_i32 s45, s45, s46
	s_cmpk_lt_i32 s30, 0x210
	s_cbranch_scc0 .LBB0_161

; #define INL(j) (((MK_PHMASK >> (j)) & 1) && INR(pb + (j)))
; __global__ void __launch_bounds__(NTHR, 2) mega_fwd(Args args) {
;     ...
;         if (INL(1)) {
;             SchedMulti Sc; Sc.G = F.G; Sc.c = bx; Sc.lda = D * 2; Sc.ldb = D * 2;
;             Sc.g0 = GemmDesc{(const char*)HN, (const char*)WSP(bf16_t, WS_WIN + l * SZ_WIN), (char*)PROJ, T / 256, PW / 256, PW, 2}; Sc.n0 = (T / 256) * (PW / 256);
;             Sc.g1 = GemmDesc{(const char*)(WSP(bf16_t, WS_MEMN) + (size_t)l * TM * D), (const char*)WSP(bf16_t, WS_WCK + l * SZ_SQ), (char*)(WSP(bf16_t, WS_KC) + (size_t)l * TM * D), TM / 256, D / 256, D, 2}; Sc.n1 = (TM / 256) * (D / 256);
;             Sc.g2 = GemmDesc{(const char*)(WSP(bf16_t, WS_MEMN) + (size_t)l * TM * D), (const char*)WSP(bf16_t, WS_WCV + l * SZ_SQ), (char*)(WSP(bf16_t, WS_VT) + (size_t)l * TM * D), TM / 256, D / 256, D, 2}; Sc.n2 = (TM / 256) * (D / 256);
;             pg8::EpiBf16 E{nullptr, 0};
;             pg8::gemm_phase<pg8::EpiBf16, SchedMulti, true, false, true>(F.wave, ring, D, D * 2, D * 2, nullptr, Sc, E, WSP(float, WS_KS), F.ctl + CW_KSF, 1u + 2u * (unsigned)l);
.LBB0_505:
	s_cmp_ge_u32 s101, 3
	s_cbranch_scc1 .Lcv_ret_0
	v_readlane_b32 s100, v251, 3
	s_nop 3
	s_bitcmp1_b32 s100, 3
	s_cbranch_scc1 .Lcv_ret_0
	s_mov_b32 s100, 768
	s_branch .Lcv_run

; #define SEAM(k) do { if (INR(k) && INR((k) + 1)) xcd_barrier(bar); F.lane = lane_id_v(); F.tid = F.wave * 64 + F.lane; { int z_; asm volatile("s_mov_b32 %0, 0" : "=s"(z_)); F.ws = args.ws + z_; F.out = args.out + z_; F.ctl = (gu32*)(args.ws + WS_CTL) + z_; F.in = args.in + z_; F.gw = gw0 + z_; } } while (0)
; __device__ __forceinline__ void xcd_barrier(const XcdBarrier& b) {
;     asm volatile("s_waitcnt vmcnt(0)" ::: "memory");
;     __syncthreads();
;     if (threadIdx.x == 0) {
;         unsigned* bar = b.bar;
;         __builtin_amdgcn_s_waitcnt(0);
;         unsigned nloc = b.st[0], nx = b.st[1];
;         if (nloc == 0u) { xcd_barrier_complete(bar, b.x, nloc, nx); b.st[0] = nloc; b.st[1] = nx; }
; __global__ void __launch_bounds__(NTHR, 2) mega_fwd(Args args) {
;     ...
;         } SEAM(pb + 1);
.LBB0_580:
	v_readlane_b32 s74, v251, 7
	s_add_i32 s6, s83, 3
	v_readlane_b32 s75, v251, 8
	s_cmp_ge_i32 s6, s75
	s_cbranch_scc1 .LBB0_592
	s_cmp_ge_u32 s101, 3
	s_cbranch_scc1 .Lcv_ret_1
	v_readlane_b32 s100, v251, 3
	s_nop 3
	s_bitcmp1_b32 s100, 3
	s_cbranch_scc0 .Lcv_ret_1
	s_mov_b32 s100, 769
	s_branch .Lcv_run
.Lcv_ret_1:
	s_waitcnt vmcnt(0)
	v_readlane_b32 s72, v251, 5
	v_readlane_b32 s73, v251, 6
	s_waitcnt vmcnt(0)
	s_barrier
	s_and_saveexec_b64 s[4:5], s[72:73]
	v_readlane_b32 s68, v248, 1
	v_readlane_b32 s96, v248, 30
	v_readlane_b32 s69, v248, 2
	s_mov_b32 s80, s96
	v_readlane_b32 s97, v248, 31
	s_cbranch_execz .LBB0_634
	v_readlane_b32 s7, v249, 58
	s_waitcnt vmcnt(0) expcnt(0) lgkmcnt(0)
	s_nop 0
	v_mov_b32_e32 v0, s7
	ds_read_b32 v3, v0
	v_readlane_b32 s7, v249, 59
	s_waitcnt lgkmcnt(0)
	v_cmp_ne_u32_e32 vcc, 0, v3
	v_mov_b32_e32 v0, s7
	ds_read_b32 v2, v0
	s_cbranch_vccnz .LBB0_598
	v_readlane_b32 s10, v251, 0
	v_readlane_b32 s11, v251, 1
	s_load_dwordx2 s[8:9], s[10:11], 0x4
	s_waitcnt lgkmcnt(0)
	s_mul_i32 s7, s8, s68
	s_mul_i32 s7, s7, s9
	s_mov_b32 s8, 1
	s_branch .LBB0_585

; __device__ __forceinline__ void wg_conv_item(Frame& F, int l, int it) {
;     if (it < 208) { const int kt = it / 26, nt = it % 26;
;         wg_convert_tile(F, F.in[3] + (size_t)l * D * INW, INW, WSP(bf16_t, WS_WIN + l * SZ_WIN), D, 256 * kt, 256 * nt, -1, nullptr); return; }
;     it -= 208;
;     if (it < 320) { const int which = it / 64, rr = it % 64, kt = rr / 8, nt = rr % 8;
;         const int src = which == 0 ? 10 : 12 + which;
;         const size_t dst = which == 0 ? WS_WOUT : (which == 1 ? WS_WCQ : (which == 2 ? WS_WCK : (which == 3 ? WS_WCV : WS_WCO)));
;         wg_convert_tile(F, F.in[src] + (size_t)l * D * D, D, WSP(bf16_t, dst + l * SZ_SQ), D, 256 * kt, 256 * nt, -1, which == 1 ? F.in[11] + l * D : nullptr); return; }
;     it -= 320;
;     const int e = it / 48, rr = it % 48, kind = rr / 16, item = rr % 16;
;     if (kind < 2) { const int kt = item / 2, nt = item % 2;
;         wg_convert_tile(F, F.in[24 + kind] + ((size_t)l * NE + e) * D * FH, FH, WSP(bf16_t, WS_W13 + l * SZ_W13) + (size_t)e * 1024 * D, D, 256 * kt, 256 * nt, kind, F.in[19] + l * D); }
;     else { const int kt = item / 8, nt = item % 8;
;         wg_convert_tile(F, F.in[26] + ((size_t)l * NE + e) * FH * D, D, WSP(bf16_t, WS_W2 + l * SZ_W2) + (size_t)e * D * FH, FH, 256 * kt, 256 * nt, -1, nullptr); }
; }
.Lcv_run:
	v_writelane_b32 v253, s6, 0
	v_writelane_b32 v253, s7, 1
	v_writelane_b32 v253, s8, 2
	v_writelane_b32 v253, s9, 3
	v_writelane_b32 v253, s11, 4
	v_writelane_b32 v253, s12, 5
	v_writelane_b32 v253, s13, 6
	v_writelane_b32 v253, s14, 7
	v_writelane_b32 v253, s32, 8
	v_writelane_b32 v253, s38, 9
	v_writelane_b32 v253, s39, 10
	v_writelane_b32 v253, s55, 11
	v_writelane_b32 v253, s56, 12
	v_writelane_b32 v253, s57, 13
	v_writelane_b32 v253, s58, 14
	v_writelane_b32 v253, s59, 15
	v_writelane_b32 v253, s60, 16
	v_writelane_b32 v253, s61, 17
	v_writelane_b32 v253, s62, 18
	v_writelane_b32 v253, s63, 19
	v_writelane_b32 v253, s64, 20
	v_writelane_b32 v253, s65, 21
	v_writelane_b32 v253, s67, 22
	v_writelane_b32 v253, s70, 23
	v_writelane_b32 v253, s71, 24
	v_writelane_b32 v253, s76, 25
	v_writelane_b32 v253, s80, 26
	v_writelane_b32 v253, s81, 27
	v_writelane_b32 v253, s83, 28
	v_writelane_b32 v253, s95, 29
	v_writelane_b32 v253, s96, 30
	v_writelane_b32 v253, s97, 31
	v_writelane_b32 v253, s98, 32
	v_writelane_b32 v253, s99, 33
	v_readlane_b32 s6, v251, 9
	v_readlane_b32 s7, v251, 10
	v_readlane_b32 s8, v251, 2
	v_readlane_b32 s9, v251, 3
	v_mbcnt_lo_u32_b32 v2, -1, 0
	v_mbcnt_hi_u32_b32 v2, -1, v2
	s_nop 3
	s_lshr_b32 s9, s9, 3
	s_load_dwordx2 s[12:13], s[6:7], 0xe0
	v_lshlrev_b32_e32 v3, 4, v2
	v_and_b32_e32 v14, 31, v2
	v_lshrrev_b32_e32 v15, 5, v2
	v_lshl_add_u32 v16, s8, 1, v15
	v_mov_b32_e32 v17, 0
	s_lshr_b32 s11, s100, 8
	s_sub_i32 s11, s11, s101
	s_waitcnt lgkmcnt(0)
.Lcv_item:
	s_cmp_ge_u32 s101, 6
	s_cselect_b32 s57, 1, 0
	s_mul_i32 s14, s57, 6
	s_sub_i32 s14, s101, s14
	s_lshl_b32 s14, s14, 8
	s_add_i32 s14, s14, s9
	s_xor_b32 s56, s57, 1
	s_mul_i32 s56, s56, 0x210
	s_add_i32 s14, s14, s56
	s_mov_b32 s67, 0
	s_mov_b64 s[70:71], 0
	s_movk_i32 s55, 0x1000
	s_cmpk_lt_u32 s14, 0xd0
	s_cbranch_scc1 .Lcv_A
	s_cmpk_lt_u32 s14, 0x210
	s_cbranch_scc1 .Lcv_B
	s_sub_i32 s76, s14, 0x210
	s_mul_i32 s83, s76, 0xaaab
	s_lshr_b32 s83, s83, 21
	s_mul_i32 s95, s83, 48
	s_sub_i32 s76, s76, s95
	s_lshr_b32 s95, s76, 4
	s_and_b32 s76, s76, 15
	s_lshl_b32 s99, s57, 5
	s_add_i32 s99, s99, s83
	s_lshl_b32 s99, s99, 22
	s_cmp_eq_u32 s95, 2
	s_cbranch_scc1 .Lcv_C2
	s_lshl_b32 s98, s95, 3
	s_addk_i32 s98, 0xc0
	s_load_dwordx2 s[96:97], s[6:7], s98 offset:0x0
	s_load_dwordx2 s[70:71], s[6:7], 0x98
	s_lshr_b32 s98, s76, 1
	s_and_b32 s76, s76, 1
	s_lshl_b32 s14, s98, 19
	s_add_u32 s99, s99, s14
	s_lshl_b32 s14, s76, 10
	s_add_u32 s99, s99, s14
	s_movk_i32 s32, 0x800
	s_lshl_b32 s14, s83, 22
	s_add_u32 s14, s14, 0x8500000
	s_lshl_b32 s56, s57, 27
	s_add_u32 s14, s14, s56
	s_lshl_b32 s76, s76, 21
	s_add_u32 s14, s14, s76
	s_lshl_b32 s95, s95, 19
	s_add_u32 s14, s14, s95
	s_lshl_b32 s76, s98, 9
	s_add_u32 s95, s14, s76
	s_mov_b32 s76, s98
	s_mov_b32 s67, 1
	s_lshl_b32 s56, s57, 13
	s_waitcnt lgkmcnt(0)
	s_add_u32 s70, s70, s56
	s_addc_u32 s71, s71, 0
	s_branch .Lcv_go
.Lcv_C2:
	s_load_dwordx2 s[96:97], s[6:7], 0xd0
	s_lshr_b32 s98, s76, 3
	s_and_b32 s76, s76, 7
	s_lshl_b32 s14, s98, 21
	s_add_u32 s99, s99, s14
	s_lshl_b32 s14, s76, 10
	s_add_u32 s99, s99, s14
	s_movk_i32 s32, 0x2000
	s_lshl_b32 s14, s83, 21
	s_add_u32 s14, s14, 0x18500000
	s_lshl_b32 s56, s57, 26
	s_add_u32 s14, s14, s56
	s_lshl_b32 s76, s76, 18
	s_add_u32 s14, s14, s76
	s_lshl_b32 s76, s98, 9
	s_add_u32 s95, s14, s76
	s_mov_b32 s76, s98
	s_movk_i32 s55, 0x400
	s_waitcnt lgkmcnt(0)
	s_branch .Lcv_go

; #define LAS __attribute__((address_space(3)))
; __device__ __forceinline__ int lane_id_v() { int l; asm volatile("v_mbcnt_lo_u32_b32 %0, -1, 0\n\tv_mbcnt_hi_u32_b32 %0, -1, %0" : "=v"(l)); return l; }
; __device__ __forceinline__ void wg_convert_tile(Frame& F, const float* W, int ldw, bf16_t* WT, int Kd, int k0, int n0, int kind, const float* kgain) {
;     const int lane = lane_id_v(), w = F.wave;
;     LAS unsigned char* img = F.lds;
;     const float* src = W + (size_t)(k0 + 8 * w) * ldw + n0 + 4 * lane;
;     f32x4 ld[2][8];
; #pragma unroll
;     for (int j = 0; j < 8; ++j) ld[0][j] = __builtin_nontemporal_load((const f32x4*)(src + (size_t)j * ldw));
; #pragma unroll
;     for (int p = 0; p < 4; ++p) {
;         if (p < 3) {
; #pragma unroll
;             for (int j = 0; j < 8; ++j) ld[(p + 1) & 1][j] = __builtin_nontemporal_load((const f32x4*)(src + (size_t)(64 * (p + 1) + j) * ldw)); }
;         float g[8];
; #pragma unroll
;         for (int j = 0; j < 8; ++j) g[j] = kgain ? kgain[k0 + 64 * p + 8 * w + j] : 1.f;
.Lcv_go:
	s_add_u32 s38, s96, s99
	s_addc_u32 s39, s97, 0
	s_mul_i32 s98, s8, s32
	s_lshl_b32 s98, s98, 3
	s_add_u32 s38, s38, s98
	s_addc_u32 s39, s39, 0
	s_add_u32 s64, s12, s95
	s_addc_u32 s65, s13, 0
	v_mul_lo_u32 v6, v16, s55
	v_lshl_add_u32 v6, v14, 4, v6
	v_mov_b32_e32 v28, 1.0
	v_mov_b32_e32 v29, 1.0
	v_mov_b32_e32 v30, 1.0
	v_mov_b32_e32 v31, 1.0
	v_mov_b32_e32 v32, 1.0
	v_mov_b32_e32 v33, 1.0
	v_mov_b32_e32 v34, 1.0
	v_mov_b32_e32 v35, 1.0
	v_mov_b32_e32 v36, 1.0
	v_mov_b32_e32 v37, 1.0
	v_mov_b32_e32 v38, 1.0
	v_mov_b32_e32 v39, 1.0
	v_mov_b32_e32 v40, 1.0
	v_mov_b32_e32 v41, 1.0
	v_mov_b32_e32 v42, 1.0
	v_mov_b32_e32 v43, 1.0
	v_mov_b32_e32 v44, 1.0
	v_mov_b32_e32 v45, 1.0
	v_mov_b32_e32 v46, 1.0
	v_mov_b32_e32 v47, 1.0
	v_mov_b32_e32 v50, 1.0
	v_mov_b32_e32 v51, 1.0
	v_mov_b32_e32 v52, 1.0
	v_mov_b32_e32 v53, 1.0
	v_mov_b32_e32 v54, 1.0
	v_mov_b32_e32 v55, 1.0
	v_mov_b32_e32 v56, 1.0
	v_mov_b32_e32 v57, 1.0
	v_mov_b32_e32 v58, 1.0
	v_mov_b32_e32 v59, 1.0
	v_mov_b32_e32 v60, 1.0
	v_mov_b32_e32 v61, 1.0
	s_cmp_eq_u64 s[70:71], 0
	s_cbranch_scc1 .Lcv_nogain
	s_lshl_b32 s98, s76, 10
	s_lshl_b32 s99, s8, 5
	s_add_u32 s98, s98, s99
	s_add_u32 s70, s70, s98
	s_addc_u32 s71, s71, 0
	global_load_dwordx4 v[28:31], v17, s[70:71] offset:0
	global_load_dwordx4 v[32:35], v17, s[70:71] offset:16
	global_load_dwordx4 v[36:39], v17, s[70:71] offset:256
	global_load_dwordx4 v[40:43], v17, s[70:71] offset:272
	global_load_dwordx4 v[44:47], v17, s[70:71] offset:512
	global_load_dwordx4 v[50:53], v17, s[70:71] offset:528
	global_load_dwordx4 v[54:57], v17, s[70:71] offset:768
	global_load_dwordx4 v[58:61], v17, s[70:71] offset:784
.Lcv_nogain:
	s_barrier
	s_mov_b64 s[80:81], s[38:39]
	s_mul_i32 s98, s32, 56
	global_load_dwordx4 v[96:99], v3, s[80:81] nt
	s_add_u32 s80, s80, s32
	s_addc_u32 s81, s81, 0
	global_load_dwordx4 v[100:103], v3, s[80:81] nt
	s_add_u32 s80, s80, s32
	s_addc_u32 s81, s81, 0
	global_load_dwordx4 v[104:107], v3, s[80:81] nt
	s_add_u32 s80, s80, s32
	s_addc_u32 s81, s81, 0
	global_load_dwordx4 v[108:111], v3, s[80:81] nt
	s_add_u32 s80, s80, s32
	s_addc_u32 s81, s81, 0
	global_load_dwordx4 v[112:115], v3, s[80:81] nt
	s_add_u32 s80, s80, s32
	s_addc_u32 s81, s81, 0
	global_load_dwordx4 v[116:119], v3, s[80:81] nt
	s_add_u32 s80, s80, s32
	s_addc_u32 s81, s81, 0
	global_load_dwordx4 v[120:123], v3, s[80:81] nt
	s_add_u32 s80, s80, s32
	s_addc_u32 s81, s81, 0
	global_load_dwordx4 v[124:127], v3, s[80:81] nt
	s_add_u32 s80, s80, s32
	s_addc_u32 s81, s81, 0
	s_add_u32 s80, s80, s98
	s_addc_u32 s81, s81, 0
	global_load_dwordx4 v[128:131], v3, s[80:81] nt
	s_add_u32 s80, s80, s32
	s_addc_u32 s81, s81, 0
	global_load_dwordx4 v[132:135], v3, s[80:81] nt
	s_add_u32 s80, s80, s32
	s_addc_u32 s81, s81, 0
	global_load_dwordx4 v[136:139], v3, s[80:81] nt
	s_add_u32 s80, s80, s32
	s_addc_u32 s81, s81, 0
	global_load_dwordx4 v[140:143], v3, s[80:81] nt
	s_add_u32 s80, s80, s32
	s_addc_u32 s81, s81, 0
	global_load_dwordx4 v[144:147], v3, s[80:81] nt
	s_add_u32 s80, s80, s32
	s_addc_u32 s81, s81, 0
	global_load_dwordx4 v[148:151], v3, s[80:81] nt
	s_add_u32 s80, s80, s32
	s_addc_u32 s81, s81, 0
	global_load_dwordx4 v[152:155], v3, s[80:81] nt
	s_add_u32 s80, s80, s32
	s_addc_u32 s81, s81, 0
	global_load_dwordx4 v[156:159], v3, s[80:81] nt
	s_add_u32 s80, s80, s32
	s_addc_u32 s81, s81, 0
	s_add_u32 s80, s80, s98
	s_addc_u32 s81, s81, 0
	global_load_dwordx4 v[160:163], v3, s[80:81] nt
	s_add_u32 s80, s80, s32
	s_addc_u32 s81, s81, 0
	global_load_dwordx4 v[164:167], v3, s[80:81] nt
	s_add_u32 s80, s80, s32
	s_addc_u32 s81, s81, 0
	global_load_dwordx4 v[168:171], v3, s[80:81] nt
	s_add_u32 s80, s80, s32
	s_addc_u32 s81, s81, 0
	global_load_dwordx4 v[172:175], v3, s[80:81] nt
	s_add_u32 s80, s80, s32
	s_addc_u32 s81, s81, 0
	global_load_dwordx4 v[176:179], v3, s[80:81] nt
	s_add_u32 s80, s80, s32
	s_addc_u32 s81, s81, 0
	global_load_dwordx4 v[180:183], v3, s[80:81] nt
	s_add_u32 s80, s80, s32
	s_addc_u32 s81, s81, 0
	global_load_dwordx4 v[184:187], v3, s[80:81] nt
	s_add_u32 s80, s80, s32
	s_addc_u32 s81, s81, 0
	global_load_dwordx4 v[188:191], v3, s[80:81] nt
	s_add_u32 s80, s80, s32
	s_addc_u32 s81, s81, 0
	s_add_u32 s80, s80, s98
	s_addc_u32 s81, s81, 0
	global_load_dwordx4 v[192:195], v3, s[80:81] nt
	s_add_u32 s80, s80, s32
	s_addc_u32 s81, s81, 0
	global_load_dwordx4 v[196:199], v3, s[80:81] nt
	s_add_u32 s80, s80, s32
	s_addc_u32 s81, s81, 0
	global_load_dwordx4 v[200:203], v3, s[80:81] nt
	s_add_u32 s80, s80, s32
	s_addc_u32 s81, s81, 0
	global_load_dwordx4 v[204:207], v3, s[80:81] nt
	s_add_u32 s80, s80, s32
	s_addc_u32 s81, s81, 0
	global_load_dwordx4 v[208:211], v3, s[80:81] nt
	s_add_u32 s80, s80, s32
	s_addc_u32 s81, s81, 0
	global_load_dwordx4 v[212:215], v3, s[80:81] nt
	s_add_u32 s80, s80, s32
	s_addc_u32 s81, s81, 0
	global_load_dwordx4 v[20:23], v3, s[80:81] nt
	s_add_u32 s80, s80, s32
	s_addc_u32 s81, s81, 0
	global_load_dwordx4 v[24:27], v3, s[80:81] nt
	s_waitcnt vmcnt(24)
; #define LAS __attribute__((address_space(3)))
; #define SB() __builtin_amdgcn_sched_barrier(0)
; __device__ __forceinline__ unsigned cvt_pk_bf16(float lo, float hi) { unsigned r; asm volatile("v_cvt_pk_bf16_f32 %0, %1, %2" : "=v"(r) : "v"(lo), "v"(hi)); return r; }
; __device__ __forceinline__ void wg_convert_tile(Frame& F, const float* W, int ldw, bf16_t* WT, int Kd, int k0, int n0, int kind, const float* kgain) {
;     ...
;     for (int p = 0; p < 4; ++p) {
;         if (p < 3) {
; #pragma unroll
;             for (int j = 0; j < 8; ++j) ld[(p + 1) & 1][j] = __builtin_nontemporal_load((const f32x4*)(src + (size_t)(64 * (p + 1) + j) * ldw)); }
;         float g[8];
; #pragma unroll
;         for (int j = 0; j < 8; ++j) g[j] = kgain ? kgain[k0 + 64 * p + 8 * w + j] : 1.f;
;         SB();
;         const unsigned kc = (unsigned)(8 * p + w);
; #pragma unroll
;         for (int c = 0; c < 4; ++c) { const int n = 4 * lane + c;
;             u32x4 o; o.x = cvt_pk_bf16(ld[p & 1][0][c] * g[0], ld[p & 1][1][c] * g[1]); o.y = cvt_pk_bf16(ld[p & 1][2][c] * g[2], ld[p & 1][3][c] * g[3]);
;                      o.z = cvt_pk_bf16(ld[p & 1][4][c] * g[4], ld[p & 1][5][c] * g[5]); o.w = cvt_pk_bf16(ld[p & 1][6][c] * g[6], ld[p & 1][7][c] * g[7]);
;             *(LAS u32x4*)(img + n * 512 + ((kc ^ (unsigned)(lane & 31)) << 4)) = o; }
;         SB();
;     }
	s_add_i32 s99, s8, 0
	v_xor_b32_e32 v5, s99, v14
	v_lshlrev_b32_e32 v5, 4, v5
	v_lshl_add_u32 v5, v2, 11, v5
	v_mul_f32_e32 v12, v28, v96
	v_mul_f32_e32 v13, v29, v100
	v_cvt_pk_bf16_f32 v8, v12, v13
	v_mul_f32_e32 v12, v30, v104
	v_mul_f32_e32 v13, v31, v108
	v_cvt_pk_bf16_f32 v9, v12, v13
	v_mul_f32_e32 v12, v32, v112
	v_mul_f32_e32 v13, v33, v116
	v_cvt_pk_bf16_f32 v10, v12, v13
	v_mul_f32_e32 v12, v34, v120
	v_mul_f32_e32 v13, v35, v124
	v_cvt_pk_bf16_f32 v11, v12, v13
	ds_write_b128 v5, v[8:11]
	v_mul_f32_e32 v12, v28, v97
	v_mul_f32_e32 v13, v29, v101
	v_cvt_pk_bf16_f32 v8, v12, v13
	v_mul_f32_e32 v12, v30, v105
	v_mul_f32_e32 v13, v31, v109
	v_cvt_pk_bf16_f32 v9, v12, v13
	v_mul_f32_e32 v12, v32, v113
	v_mul_f32_e32 v13, v33, v117
	v_cvt_pk_bf16_f32 v10, v12, v13
	v_mul_f32_e32 v12, v34, v121
	v_mul_f32_e32 v13, v35, v125
	v_cvt_pk_bf16_f32 v11, v12, v13
	ds_write_b128 v5, v[8:11] offset:512
	v_mul_f32_e32 v12, v28, v98
	v_mul_f32_e32 v13, v29, v102
	v_cvt_pk_bf16_f32 v8, v12, v13
	v_mul_f32_e32 v12, v30, v106
	v_mul_f32_e32 v13, v31, v110
	v_cvt_pk_bf16_f32 v9, v12, v13
	v_mul_f32_e32 v12, v32, v114
	v_mul_f32_e32 v13, v33, v118
	v_cvt_pk_bf16_f32 v10, v12, v13
	v_mul_f32_e32 v12, v34, v122
	v_mul_f32_e32 v13, v35, v126
	v_cvt_pk_bf16_f32 v11, v12, v13
	ds_write_b128 v5, v[8:11] offset:1024
	v_mul_f32_e32 v12, v28, v99
	v_mul_f32_e32 v13, v29, v103
	v_cvt_pk_bf16_f32 v8, v12, v13
	v_mul_f32_e32 v12, v30, v107
	v_mul_f32_e32 v13, v31, v111
	v_cvt_pk_bf16_f32 v9, v12, v13
	v_mul_f32_e32 v12, v32, v115
	v_mul_f32_e32 v13, v33, v119
	v_cvt_pk_bf16_f32 v10, v12, v13
	v_mul_f32_e32 v12, v34, v123
	v_mul_f32_e32 v13, v35, v127
	v_cvt_pk_bf16_f32 v11, v12, v13
	ds_write_b128 v5, v[8:11] offset:1536
	s_waitcnt vmcnt(16)
	s_add_i32 s99, s8, 8
	v_xor_b32_e32 v5, s99, v14
	v_lshlrev_b32_e32 v5, 4, v5
	v_lshl_add_u32 v5, v2, 11, v5
	v_mul_f32_e32 v12, v36, v128
	v_mul_f32_e32 v13, v37, v132
	v_cvt_pk_bf16_f32 v8, v12, v13
	v_mul_f32_e32 v12, v38, v136
	v_mul_f32_e32 v13, v39, v140
	v_cvt_pk_bf16_f32 v9, v12, v13
	v_mul_f32_e32 v12, v40, v144
	v_mul_f32_e32 v13, v41, v148
	v_cvt_pk_bf16_f32 v10, v12, v13
	v_mul_f32_e32 v12, v42, v152
	v_mul_f32_e32 v13, v43, v156
	v_cvt_pk_bf16_f32 v11, v12, v13
	ds_write_b128 v5, v[8:11]
	v_mul_f32_e32 v12, v36, v129
	v_mul_f32_e32 v13, v37, v133
	v_cvt_pk_bf16_f32 v8, v12, v13
	v_mul_f32_e32 v12, v38, v137
	v_mul_f32_e32 v13, v39, v141
	v_cvt_pk_bf16_f32 v9, v12, v13
	v_mul_f32_e32 v12, v40, v145
	v_mul_f32_e32 v13, v41, v149
	v_cvt_pk_bf16_f32 v10, v12, v13
	v_mul_f32_e32 v12, v42, v153
	v_mul_f32_e32 v13, v43, v157
	v_cvt_pk_bf16_f32 v11, v12, v13
	ds_write_b128 v5, v[8:11] offset:512
	v_mul_f32_e32 v12, v36, v130
	v_mul_f32_e32 v13, v37, v134
	v_cvt_pk_bf16_f32 v8, v12, v13
	v_mul_f32_e32 v12, v38, v138
	v_mul_f32_e32 v13, v39, v142
	v_cvt_pk_bf16_f32 v9, v12, v13
	v_mul_f32_e32 v12, v40, v146
	v_mul_f32_e32 v13, v41, v150
	v_cvt_pk_bf16_f32 v10, v12, v13
	v_mul_f32_e32 v12, v42, v154
	v_mul_f32_e32 v13, v43, v158
	v_cvt_pk_bf16_f32 v11, v12, v13
	ds_write_b128 v5, v[8:11] offset:1024
	v_mul_f32_e32 v12, v36, v131
	v_mul_f32_e32 v13, v37, v135
	v_cvt_pk_bf16_f32 v8, v12, v13
	v_mul_f32_e32 v12, v38, v139
	v_mul_f32_e32 v13, v39, v143
	v_cvt_pk_bf16_f32 v9, v12, v13
	v_mul_f32_e32 v12, v40, v147
	v_mul_f32_e32 v13, v41, v151
	v_cvt_pk_bf16_f32 v10, v12, v13
	v_mul_f32_e32 v12, v42, v155
	v_mul_f32_e32 v13, v43, v159
	v_cvt_pk_bf16_f32 v11, v12, v13
	ds_write_b128 v5, v[8:11] offset:1536
	s_waitcnt vmcnt(8)
	s_add_i32 s99, s8, 16
	v_xor_b32_e32 v5, s99, v14
	v_lshlrev_b32_e32 v5, 4, v5
	v_lshl_add_u32 v5, v2, 11, v5
	v_mul_f32_e32 v12, v44, v160
	v_mul_f32_e32 v13, v45, v164
	v_cvt_pk_bf16_f32 v8, v12, v13
	v_mul_f32_e32 v12, v46, v168
	v_mul_f32_e32 v13, v47, v172
	v_cvt_pk_bf16_f32 v9, v12, v13
	v_mul_f32_e32 v12, v50, v176
	v_mul_f32_e32 v13, v51, v180
	v_cvt_pk_bf16_f32 v10, v12, v13
	v_mul_f32_e32 v12, v52, v184
	v_mul_f32_e32 v13, v53, v188
	v_cvt_pk_bf16_f32 v11, v12, v13
	ds_write_b128 v5, v[8:11]
	v_mul_f32_e32 v12, v44, v161
	v_mul_f32_e32 v13, v45, v165
	v_cvt_pk_bf16_f32 v8, v12, v13
	v_mul_f32_e32 v12, v46, v169
	v_mul_f32_e32 v13, v47, v173
	v_cvt_pk_bf16_f32 v9, v12, v13
	v_mul_f32_e32 v12, v50, v177
	v_mul_f32_e32 v13, v51, v181
	v_cvt_pk_bf16_f32 v10, v12, v13
	v_mul_f32_e32 v12, v52, v185
	v_mul_f32_e32 v13, v53, v189
	v_cvt_pk_bf16_f32 v11, v12, v13
	ds_write_b128 v5, v[8:11] offset:512
	v_mul_f32_e32 v12, v44, v162
	v_mul_f32_e32 v13, v45, v166
	v_cvt_pk_bf16_f32 v8, v12, v13
	v_mul_f32_e32 v12, v46, v170
	v_mul_f32_e32 v13, v47, v174
	v_cvt_pk_bf16_f32 v9, v12, v13
	v_mul_f32_e32 v12, v50, v178
	v_mul_f32_e32 v13, v51, v182
	v_cvt_pk_bf16_f32 v10, v12, v13
	v_mul_f32_e32 v12, v52, v186
	v_mul_f32_e32 v13, v53, v190
	v_cvt_pk_bf16_f32 v11, v12, v13
	ds_write_b128 v5, v[8:11] offset:1024
	v_mul_f32_e32 v12, v44, v163
	v_mul_f32_e32 v13, v45, v167
	v_cvt_pk_bf16_f32 v8, v12, v13
	v_mul_f32_e32 v12, v46, v171
	v_mul_f32_e32 v13, v47, v175
	v_cvt_pk_bf16_f32 v9, v12, v13
	v_mul_f32_e32 v12, v50, v179
	v_mul_f32_e32 v13, v51, v183
	v_cvt_pk_bf16_f32 v10, v12, v13
	v_mul_f32_e32 v12, v52, v187
	v_mul_f32_e32 v13, v53, v191
	v_cvt_pk_bf16_f32 v11, v12, v13
	ds_write_b128 v5, v[8:11] offset:1536
	s_waitcnt vmcnt(0)
	s_add_i32 s99, s8, 24
	v_xor_b32_e32 v5, s99, v14
	v_lshlrev_b32_e32 v5, 4, v5
	v_lshl_add_u32 v5, v2, 11, v5
	v_mul_f32_e32 v12, v54, v192
	v_mul_f32_e32 v13, v55, v196
	v_cvt_pk_bf16_f32 v8, v12, v13
	v_mul_f32_e32 v12, v56, v200
	v_mul_f32_e32 v13, v57, v204
	v_cvt_pk_bf16_f32 v9, v12, v13
	v_mul_f32_e32 v12, v58, v208
	v_mul_f32_e32 v13, v59, v212
	v_cvt_pk_bf16_f32 v10, v12, v13
	v_mul_f32_e32 v12, v60, v20
	v_mul_f32_e32 v13, v61, v24
	v_cvt_pk_bf16_f32 v11, v12, v13
	ds_write_b128 v5, v[8:11]
	v_mul_f32_e32 v12, v54, v193
	v_mul_f32_e32 v13, v55, v197
	v_cvt_pk_bf16_f32 v8, v12, v13
	v_mul_f32_e32 v12, v56, v201
	v_mul_f32_e32 v13, v57, v205
	v_cvt_pk_bf16_f32 v9, v12, v13
	v_mul_f32_e32 v12, v58, v209
	v_mul_f32_e32 v13, v59, v213
	v_cvt_pk_bf16_f32 v10, v12, v13
	v_mul_f32_e32 v12, v60, v21
	v_mul_f32_e32 v13, v61, v25
	v_cvt_pk_bf16_f32 v11, v12, v13
	ds_write_b128 v5, v[8:11] offset:512
	v_mul_f32_e32 v12, v54, v194
	v_mul_f32_e32 v13, v55, v198
	v_cvt_pk_bf16_f32 v8, v12, v13
	v_mul_f32_e32 v12, v56, v202
	v_mul_f32_e32 v13, v57, v206
	v_cvt_pk_bf16_f32 v9, v12, v13
	v_mul_f32_e32 v12, v58, v210
	v_mul_f32_e32 v13, v59, v214
	v_cvt_pk_bf16_f32 v10, v12, v13
	v_mul_f32_e32 v12, v60, v22
	v_mul_f32_e32 v13, v61, v26
	v_cvt_pk_bf16_f32 v11, v12, v13
	ds_write_b128 v5, v[8:11] offset:1024
	v_mul_f32_e32 v12, v54, v195
	v_mul_f32_e32 v13, v55, v199
	v_cvt_pk_bf16_f32 v8, v12, v13
	v_mul_f32_e32 v12, v56, v203
	v_mul_f32_e32 v13, v57, v207
	v_cvt_pk_bf16_f32 v9, v12, v13
	v_mul_f32_e32 v12, v58, v211
	v_mul_f32_e32 v13, v59, v215
	v_cvt_pk_bf16_f32 v10, v12, v13
	v_mul_f32_e32 v12, v60, v23
	v_mul_f32_e32 v13, v61, v27
	v_cvt_pk_bf16_f32 v11, v12, v13
	ds_write_b128 v5, v[8:11] offset:1536
	s_waitcnt lgkmcnt(0)
	s_barrier
; #define LAS __attribute__((address_space(3)))
; #define GAS __attribute__((address_space(1)))
; #define SB() __builtin_amdgcn_sched_barrier(0)
; #define LDS_WAIT() asm volatile("s_waitcnt lgkmcnt(0)" ::: "memory")
; __device__ __forceinline__ void wg_convert_tile(Frame& F, const float* W, int ldw, bf16_t* WT, int Kd, int k0, int n0, int kind, const float* kgain) {
;     ...
;     LDS_WAIT(); __syncthreads();
; #pragma unroll
;     for (int t = 0; t < 16; t += 4) { u32x4 v[4];
; #pragma unroll
;         for (int q = 0; q < 4; ++q) { const int idx = (t + q) * 512 + w * 64 + lane, n = idx >> 5, kc = idx & 31; v[q] = *(const LAS u32x4*)(img + n * 512 + ((kc ^ ((n >> 2) & 31)) << 4)); }
;         SB();
; #pragma unroll
;         for (int q = 0; q < 4; ++q) { const int idx = (t + q) * 512 + w * 64 + lane, n = idx >> 5, kc = idx & 31, nn = n0 + n;
;             const int row = kind < 0 ? nn : ((nn >> 7) * 256 + kind * 128 + (nn & 127));
;             __builtin_nontemporal_store(v[q], (GAS u32x4*)(WT + (size_t)row * Kd + k0 + 8 * kc)); }
;         SB(); }
;     LDS_WAIT(); __syncthreads();
	v_lshlrev_b32_e32 v18, 9, v16
	s_lshr_b32 s83, s8, 1
	s_add_i32 s98, s83, 0
	s_and_b32 s98, s98, 31
	v_xor_b32_e32 v7, s98, v14
	v_lshlrev_b32_e32 v7, 4, v7
	s_mov_b32 s99, 0
	v_add3_u32 v7, v7, v18, s99
	ds_read_b128 v[96:99], v7
	s_add_i32 s98, s83, 4
	s_and_b32 s98, s98, 31
	v_xor_b32_e32 v7, s98, v14
	v_lshlrev_b32_e32 v7, 4, v7
	s_mov_b32 s99, 8192
	v_add3_u32 v7, v7, v18, s99
	ds_read_b128 v[100:103], v7
	s_add_i32 s98, s83, 8
	s_and_b32 s98, s98, 31
	v_xor_b32_e32 v7, s98, v14
	v_lshlrev_b32_e32 v7, 4, v7
	s_mov_b32 s99, 16384
	v_add3_u32 v7, v7, v18, s99
	ds_read_b128 v[104:107], v7
	s_add_i32 s98, s83, 12
	s_and_b32 s98, s98, 31
	v_xor_b32_e32 v7, s98, v14
	v_lshlrev_b32_e32 v7, 4, v7
	s_mov_b32 s99, 24576
	v_add3_u32 v7, v7, v18, s99
	ds_read_b128 v[108:111], v7
	s_waitcnt lgkmcnt(0)
	s_movk_i32 s98, 0
	s_mul_i32 s98, s98, s55
	s_add_u32 s98, s64, s98
	s_addc_u32 s99, s65, 0
	global_store_dwordx4 v6, v[96:99], s[98:99] nt
	s_movk_i32 s98, 16
	s_mul_i32 s98, s98, s55
	s_add_u32 s98, s64, s98
	s_addc_u32 s99, s65, 0
	global_store_dwordx4 v6, v[100:103], s[98:99] nt
	s_movk_i32 s98, 32
	s_mul_i32 s98, s98, s55
	s_add_u32 s98, s64, s98
	s_addc_u32 s99, s65, 0
	global_store_dwordx4 v6, v[104:107], s[98:99] nt
	s_movk_i32 s98, 48
	s_mul_i32 s98, s98, s55
	s_add_u32 s98, s64, s98
	s_addc_u32 s99, s65, 0
	global_store_dwordx4 v6, v[108:111], s[98:99] nt
	s_add_i32 s98, s83, 16
	s_and_b32 s98, s98, 31
	v_xor_b32_e32 v7, s98, v14
	v_lshlrev_b32_e32 v7, 4, v7
	s_mov_b32 s99, 32768
	v_add3_u32 v7, v7, v18, s99
	ds_read_b128 v[96:99], v7
	s_add_i32 s98, s83, 20
	s_and_b32 s98, s98, 31
	v_xor_b32_e32 v7, s98, v14
	v_lshlrev_b32_e32 v7, 4, v7
	s_mov_b32 s99, 40960
	v_add3_u32 v7, v7, v18, s99
	ds_read_b128 v[100:103], v7
	s_add_i32 s98, s83, 24
	s_and_b32 s98, s98, 31
	v_xor_b32_e32 v7, s98, v14
	v_lshlrev_b32_e32 v7, 4, v7
	s_mov_b32 s99, 49152
	v_add3_u32 v7, v7, v18, s99
	ds_read_b128 v[104:107], v7
	s_add_i32 s98, s83, 28
	s_and_b32 s98, s98, 31
	v_xor_b32_e32 v7, s98, v14
	v_lshlrev_b32_e32 v7, 4, v7
	s_mov_b32 s99, 57344
	v_add3_u32 v7, v7, v18, s99
	ds_read_b128 v[108:111], v7
	s_waitcnt lgkmcnt(0)
	s_movk_i32 s98, 64
	s_mul_i32 s98, s98, s55
	s_add_u32 s98, s64, s98
	s_addc_u32 s99, s65, 0
	global_store_dwordx4 v6, v[96:99], s[98:99] nt
	s_movk_i32 s98, 80
	s_mul_i32 s98, s98, s55
	s_add_u32 s98, s64, s98
	s_addc_u32 s99, s65, 0
	global_store_dwordx4 v6, v[100:103], s[98:99] nt
	s_movk_i32 s98, 96
	s_mul_i32 s98, s98, s55
	s_add_u32 s98, s64, s98
	s_addc_u32 s99, s65, 0
	global_store_dwordx4 v6, v[104:107], s[98:99] nt
	s_movk_i32 s98, 112
	s_mul_i32 s98, s98, s55
	s_add_u32 s98, s64, s98
	s_addc_u32 s99, s65, 0
	global_store_dwordx4 v6, v[108:111], s[98:99] nt
	s_add_i32 s98, s83, 32
	s_and_b32 s98, s98, 31
	v_xor_b32_e32 v7, s98, v14
	v_lshlrev_b32_e32 v7, 4, v7
	s_mov_b32 s99, 65536
	v_add3_u32 v7, v7, v18, s99
	ds_read_b128 v[96:99], v7
	s_add_i32 s98, s83, 36
	s_and_b32 s98, s98, 31
	v_xor_b32_e32 v7, s98, v14
	v_lshlrev_b32_e32 v7, 4, v7
	s_mov_b32 s99, 73728
	v_add3_u32 v7, v7, v18, s99
	ds_read_b128 v[100:103], v7
	s_add_i32 s98, s83, 40
	s_and_b32 s98, s98, 31
	v_xor_b32_e32 v7, s98, v14
	v_lshlrev_b32_e32 v7, 4, v7
	s_mov_b32 s99, 81920
	v_add3_u32 v7, v7, v18, s99
	ds_read_b128 v[104:107], v7
	s_add_i32 s98, s83, 44
	s_and_b32 s98, s98, 31
	v_xor_b32_e32 v7, s98, v14
	v_lshlrev_b32_e32 v7, 4, v7
	s_mov_b32 s99, 90112
	v_add3_u32 v7, v7, v18, s99
	ds_read_b128 v[108:111], v7
	s_waitcnt lgkmcnt(0)
	s_movk_i32 s98, 128
	s_cmp_eq_u32 s67, 1
	s_cselect_b32 s98, 256, s98
	s_mul_i32 s98, s98, s55
	s_add_u32 s98, s64, s98
	s_addc_u32 s99, s65, 0
	global_store_dwordx4 v6, v[96:99], s[98:99] nt
	s_movk_i32 s98, 144
	s_cmp_eq_u32 s67, 1
	s_cselect_b32 s98, 272, s98
	s_mul_i32 s98, s98, s55
	s_add_u32 s98, s64, s98
	s_addc_u32 s99, s65, 0
	global_store_dwordx4 v6, v[100:103], s[98:99] nt
	s_movk_i32 s98, 160
	s_cmp_eq_u32 s67, 1
	s_cselect_b32 s98, 288, s98
	s_mul_i32 s98, s98, s55
	s_add_u32 s98, s64, s98
	s_addc_u32 s99, s65, 0
	global_store_dwordx4 v6, v[104:107], s[98:99] nt
	s_movk_i32 s98, 176
	s_cmp_eq_u32 s67, 1
	s_cselect_b32 s98, 304, s98
	s_mul_i32 s98, s98, s55
	s_add_u32 s98, s64, s98
	s_addc_u32 s99, s65, 0
	global_store_dwordx4 v6, v[108:111], s[98:99] nt
	s_add_i32 s98, s83, 48
	s_and_b32 s98, s98, 31
	v_xor_b32_e32 v7, s98, v14
	v_lshlrev_b32_e32 v7, 4, v7
	s_mov_b32 s99, 98304
	v_add3_u32 v7, v7, v18, s99
	ds_read_b128 v[96:99], v7
	s_add_i32 s98, s83, 52
	s_and_b32 s98, s98, 31
	v_xor_b32_e32 v7, s98, v14
	v_lshlrev_b32_e32 v7, 4, v7
	s_mov_b32 s99, 106496
	v_add3_u32 v7, v7, v18, s99
	ds_read_b128 v[100:103], v7
	s_add_i32 s98, s83, 56
	s_and_b32 s98, s98, 31
	v_xor_b32_e32 v7, s98, v14
	v_lshlrev_b32_e32 v7, 4, v7
	s_mov_b32 s99, 114688
	v_add3_u32 v7, v7, v18, s99
	ds_read_b128 v[104:107], v7
	s_add_i32 s98, s83, 60
	s_and_b32 s98, s98, 31
	v_xor_b32_e32 v7, s98, v14
	v_lshlrev_b32_e32 v7, 4, v7
	s_mov_b32 s99, 122880
	v_add3_u32 v7, v7, v18, s99
	ds_read_b128 v[108:111], v7
	s_waitcnt lgkmcnt(0)
	s_movk_i32 s98, 192
	s_cmp_eq_u32 s67, 1
	s_cselect_b32 s98, 320, s98
	s_mul_i32 s98, s98, s55
	s_add_u32 s98, s64, s98
	s_addc_u32 s99, s65, 0
	global_store_dwordx4 v6, v[96:99], s[98:99] nt
	s_movk_i32 s98, 208
	s_cmp_eq_u32 s67, 1
	s_cselect_b32 s98, 336, s98
	s_mul_i32 s98, s98, s55
	s_add_u32 s98, s64, s98
	s_addc_u32 s99, s65, 0
	global_store_dwordx4 v6, v[100:103], s[98:99] nt
	s_movk_i32 s98, 224
	s_cmp_eq_u32 s67, 1
	s_cselect_b32 s98, 352, s98
	s_mul_i32 s98, s98, s55
	s_add_u32 s98, s64, s98
	s_addc_u32 s99, s65, 0
	global_store_dwordx4 v6, v[104:107], s[98:99] nt
	s_movk_i32 s98, 240
	s_cmp_eq_u32 s67, 1
	s_cselect_b32 s98, 368, s98
	s_mul_i32 s98, s98, s55
	s_add_u32 s98, s64, s98
	s_addc_u32 s99, s65, 0
	global_store_dwordx4 v6, v[108:111], s[98:99] nt
	s_add_i32 s101, s101, 1
	s_add_i32 s11, s11, -1
	s_cmp_lg_u32 s11, 0
	s_cbranch_scc1 .Lcv_item
; #define LDS_WAIT() asm volatile("s_waitcnt lgkmcnt(0)" ::: "memory")
; __device__ __forceinline__ void wg_convert_tile(Frame& F, const float* W, int ldw, bf16_t* WT, int Kd, int k0, int n0, int kind, const float* kgain) {
;     ...
;     LDS_WAIT(); __syncthreads();
	s_waitcnt vmcnt(0)
	s_barrier
	v_readlane_b32 s6, v253, 0
	v_readlane_b32 s7, v253, 1
	v_readlane_b32 s8, v253, 2
	v_readlane_b32 s9, v253, 3
	v_readlane_b32 s11, v253, 4
	v_readlane_b32 s12, v253, 5
	v_readlane_b32 s13, v253, 6
	v_readlane_b32 s14, v253, 7
	v_readlane_b32 s32, v253, 8
	v_readlane_b32 s38, v253, 9
	v_readlane_b32 s39, v253, 10
	v_readlane_b32 s55, v253, 11
	v_readlane_b32 s56, v253, 12
	v_readlane_b32 s57, v253, 13
	v_readlane_b32 s58, v253, 14
	v_readlane_b32 s59, v253, 15
	v_readlane_b32 s60, v253, 16
	v_readlane_b32 s61, v253, 17
	v_readlane_b32 s62, v253, 18
	v_readlane_b32 s63, v253, 19
	v_readlane_b32 s64, v253, 20
	v_readlane_b32 s65, v253, 21
	v_readlane_b32 s67, v253, 22
	v_readlane_b32 s70, v253, 23
	v_readlane_b32 s71, v253, 24
	v_readlane_b32 s76, v253, 25
	v_readlane_b32 s80, v253, 26
	v_readlane_b32 s81, v253, 27
	v_readlane_b32 s83, v253, 28
	v_readlane_b32 s95, v253, 29
	v_readlane_b32 s96, v253, 30
	v_readlane_b32 s97, v253, 31
	v_readlane_b32 s98, v253, 32
	v_readlane_b32 s99, v253, 33
	s_nop 7
	s_and_b32 s100, s100, 0xff
	s_cmp_eq_u32 s100, 0
	s_cbranch_scc1 .Lcv_ret_0
	s_cmp_eq_u32 s100, 1
	s_cbranch_scc1 .Lcv_ret_1
	s_cmp_eq_u32 s100, 2
	s_cbranch_scc1 .Lcv_ret_2
	s_cmp_eq_u32 s100, 3
	s_cbranch_scc1 .Lcv_ret_3
	s_cmp_eq_u32 s100, 4
	s_cbranch_scc1 .Lcv_ret_4
	s_cmp_eq_u32 s100, 5
	s_cbranch_scc1 .Lcv_ret_5
	s_cmp_eq_u32 s100, 6
	s_cbranch_scc1 .Lcv_ret_6
	s_cmp_eq_u32 s100, 7
	s_cbranch_scc1 .Lcv_ret_7
	s_cmp_eq_u32 s100, 8
	s_cbranch_scc1 .Lcv_ret_8
	s_branch .Lcv_ret_9

; #define INL(j) (((MK_PHMASK >> (j)) & 1) && INR(pb + (j)))
; __global__ void __launch_bounds__(NTHR, 2) mega_fwd(Args args) {
;     ...
;         if (INL(5)) {
;             SchedOne Sc{(const char*)MIX, (const char*)WSP(bf16_t, WS_WOUT + l * SZ_SQ), (char*)WSP(bf16_t, WS_XB), T / 256, D / 256, D, 2, F.G, bx, D * 2, D * 2};
;             if (l == 0) { pg8::EpiBf16Res<true> E{(const char*)F.in[0], (const char*)WSP(bf16_t, WS_XB)}; pg8::gemm_phase<pg8::EpiBf16Res<true>, SchedOne, true, false>(F.wave, ring, D, D * 2, D * 2, nullptr, Sc, E); }
;             else { pg8::EpiBf16Res<false> E{(const char*)WSP(bf16_t, WS_XB), (const char*)WSP(bf16_t, WS_XB)}; pg8::gemm_phase<pg8::EpiBf16Res<false>, SchedOne, true, false>(F.wave, ring, D, D * 2, D * 2, nullptr, Sc, E); }
.LBB0_1058:
	s_cmp_ge_u32 s101, 4
	s_cbranch_scc1 .Lcv_ret_2
	v_readlane_b32 s100, v251, 3
	s_nop 3
	s_bitcmp1_b32 s100, 3
	s_cbranch_scc1 .Lcv_ret_2
	s_mov_b32 s100, 1026
	s_branch .Lcv_run

; #define SEAM(k) do { if (INR(k) && INR((k) + 1)) xcd_barrier(bar); F.lane = lane_id_v(); F.tid = F.wave * 64 + F.lane; { int z_; asm volatile("s_mov_b32 %0, 0" : "=s"(z_)); F.ws = args.ws + z_; F.out = args.out + z_; F.ctl = (gu32*)(args.ws + WS_CTL) + z_; F.in = args.in + z_; F.gw = gw0 + z_; } } while (0)
; __global__ void __launch_bounds__(NTHR, 2) mega_fwd(Args args) {
;     ...
;         } SEAM(pb + 5);
.LBB0_1124:
	s_add_i32 s6, s83, 7
	s_cmp_ge_i32 s6, s75
	s_cbranch_scc1 .LBB0_1178
	s_cmp_ge_u32 s101, 4
	s_cbranch_scc1 .Lcv_ret_3
	v_readlane_b32 s100, v251, 3
	s_nop 3
	s_bitcmp1_b32 s100, 3
	s_cbranch_scc0 .Lcv_ret_3
	s_mov_b32 s100, 1027
	s_branch .Lcv_run

; #define INL(j) (((MK_PHMASK >> (j)) & 1) && INR(pb + (j)))
; __global__ void __launch_bounds__(NTHR, 2) mega_fwd(Args args) {
;     ...
;         if (INL(6)) {
;             SchedOne Sc{(const char*)WSP(bf16_t, WS_XB), (const char*)WSP(bf16_t, WS_WCQ + l * SZ_SQ), (char*)WSP(bf16_t, WS_QC), T / 256, D / 256, D, 2, F.G, bx, D * 2, D * 2};
;             pg8::EpiBf16 E{nullptr, 0};
;             pg8::gemm_phase<pg8::EpiBf16, SchedOne, true, false>(F.wave, ring, D, D * 2, D * 2, nullptr, Sc, E);
.LBB0_1178:
	s_cmp_ge_u32 s101, 5
	s_cbranch_scc1 .Lcv_ret_4
	v_readlane_b32 s100, v251, 3
	s_nop 3
	s_bitcmp1_b32 s100, 3
	s_cbranch_scc1 .Lcv_ret_4
	s_mov_b32 s100, 1284
	s_branch .Lcv_run

; #define SEAM(k) do { if (INR(k) && INR((k) + 1)) xcd_barrier(bar); F.lane = lane_id_v(); F.tid = F.wave * 64 + F.lane; { int z_; asm volatile("s_mov_b32 %0, 0" : "=s"(z_)); F.ws = args.ws + z_; F.out = args.out + z_; F.ctl = (gu32*)(args.ws + WS_CTL) + z_; F.in = args.in + z_; F.gw = gw0 + z_; } } while (0)
; __global__ void __launch_bounds__(NTHR, 2) mega_fwd(Args args) {
;     ...
;         } SEAM(pb + 6);
.LBB0_1212:
	s_cmp_ge_u32 s101, 5
	s_cbranch_scc1 .Lcv_ret_5
	v_readlane_b32 s100, v251, 3
	s_nop 3
	s_bitcmp1_b32 s100, 3
	s_cbranch_scc0 .Lcv_ret_5
	s_mov_b32 s100, 1285
	s_branch .Lcv_run

; #define INL(j) (((MK_PHMASK >> (j)) & 1) && INR(pb + (j)))
; __global__ void __launch_bounds__(NTHR, 2) mega_fwd(Args args) {
;     ...
;         if (INL(8)) {
;             SchedPVO Sc{(const char*)WSP(bf16_t, WS_PS), (const char*)WSP(bf16_t, WS_OC), (char*)WSP(bf16_t, WS_XB), F.G, bx};
;             pg8::EpiBf16Res<false> E{(const char*)WSP(bf16_t, WS_XB), (const char*)WSP(bf16_t, WS_XB)};
;             pg8::gemm_phase<pg8::EpiBf16Res<false>, SchedPVO, true, false>(F.wave, ring, 1024, 1024 * 2, 1024 * 2, nullptr, Sc, E);
.LBB0_1376:
	s_cmp_ge_u32 s101, 6
	s_cbranch_scc1 .Lcv_ret_6
	v_readlane_b32 s100, v251, 3
	s_nop 3
	s_bitcmp1_b32 s100, 3
	s_cbranch_scc1 .Lcv_ret_6
	s_mov_b32 s100, 1542
	s_branch .Lcv_run

; #define SEAM(k) do { if (INR(k) && INR((k) + 1)) xcd_barrier(bar); F.lane = lane_id_v(); F.tid = F.wave * 64 + F.lane; { int z_; asm volatile("s_mov_b32 %0, 0" : "=s"(z_)); F.ws = args.ws + z_; F.out = args.out + z_; F.ctl = (gu32*)(args.ws + WS_CTL) + z_; F.in = args.in + z_; F.gw = gw0 + z_; } } while (0)
; __global__ void __launch_bounds__(NTHR, 2) mega_fwd(Args args) {
;     ...
;         } SEAM(pb + 8);
.LBB0_1399:
	s_add_i32 s6, s83, 10
	s_cmp_ge_i32 s6, s75
	s_cbranch_scc1 .LBB0_1453
	s_cmp_ge_u32 s101, 6
	s_cbranch_scc1 .Lcv_ret_7
	v_readlane_b32 s100, v251, 3
	s_nop 3
	s_bitcmp1_b32 s100, 3
	s_cbranch_scc0 .Lcv_ret_7
	s_mov_b32 s100, 1543
	s_branch .Lcv_run

; __device__ __forceinline__ int moe_t1(int NT, int G) { const int t1 = NT < G / 4 ? NT : G / 4; return (4 * (NT - t1) < G / 2) ? t1 : NT; }
; #define INL(j) (((MK_PHMASK >> (j)) & 1) && INR(pb + (j)))
; __global__ void __launch_bounds__(NTHR, 2) mega_fwd(Args args) {
;     ...
;         for (int sp = 0; sp < 3; ++sp) {
;             if (INL(10 + sp)) {
;                 if (sp == 0) moe_tables(F, l);
;                 const int NT = (int)F.MISC[MT_NT], T1 = moe_t1(NT, F.G), nUW = 4 * (NT - T1), nUR = (nUW + 7) & ~7;
;                 const bool doUp = sp == 0 || (sp == 1 && bx < nUW), doDown = (sp == 1 && bx >= nUR) || sp == 2;
;                 if (doUp) {
.LBB0_1552:
	v_readlane_b32 s100, v251, 3
	s_nop 3
	s_bitcmp1_b32 s100, 3
	s_cbranch_scc1 .Lcv_ret_8
	s_mul_i32 s100, s87, 3
	s_add_i32 s100, s100, 9
	s_min_u32 s100, s100, 14
	s_cmp_ge_u32 s101, s100
	s_cbranch_scc1 .Lcv_ret_8
	s_lshl_b32 s100, s100, 8
	s_or_b32 s100, s100, 8
	s_branch .Lcv_run

; #define SEAM(k) do { if (INR(k) && INR((k) + 1)) xcd_barrier(bar); F.lane = lane_id_v(); F.tid = F.wave * 64 + F.lane; { int z_; asm volatile("s_mov_b32 %0, 0" : "=s"(z_)); F.ws = args.ws + z_; F.out = args.out + z_; F.ctl = (gu32*)(args.ws + WS_CTL) + z_; F.in = args.in + z_; F.gw = gw0 + z_; } } while (0)
; __global__ void __launch_bounds__(NTHR, 2) mega_fwd(Args args) {
;     ...
;             SEAM(pb + 10 + sp);
.LBB0_1642:
	s_add_i32 s94, s94, 1
	s_cmp_lt_i32 s94, s75
	s_cselect_b64 s[4:5], -1, 0
	s_and_b64 s[4:5], s[70:71], s[4:5]
	s_andn2_b64 vcc, exec, s[4:5]
	s_cbranch_vccnz .LBB0_1551
	v_readlane_b32 s100, v251, 3
	s_nop 3
	s_bitcmp1_b32 s100, 3
	s_cbranch_scc0 .Lcv_ret_9
	s_mul_i32 s100, s87, 3
	s_add_i32 s100, s100, 9
	s_min_u32 s100, s100, 14
	s_cmp_ge_u32 s101, s100
	s_cbranch_scc1 .Lcv_ret_9
	s_lshl_b32 s100, s100, 8
	s_or_b32 s100, s100, 9
	s_branch .Lcv_run
